# prep hand-rewrite: single kernarg load, global (not flat) prefetch after critical loads, DPP/permlane reduce, v.bias folded into block 0
# baseline (speedup 1.0000x reference)
_Z11prep_kernelPKfS0_S0_S0_Pf:
	s_load_dwordx8 s[4:11], s[0:1], 0x0
	s_load_dwordx2 s[12:13], s[0:1], 0x20
	s_cmpk_eq_i32 s2, 0x100
	s_cbranch_scc1 .Lprep_done
	s_and_b32 s14, s2, 63
	s_lshr_b32 s15, s2, 6
	v_and_b32_e32 v1, 7, v0
	v_and_b32_e32 v2, 0x3f8, v0
	v_lshlrev_b32_e32 v3, 10, v2
	v_lshl_or_b32 v3, v1, 4, v3
	s_lshl_b32 s16, s15, 21
	s_lshl_b32 s17, s14, 7
	s_add_i32 s16, s16, s17
	v_add_u32_e32 v3, s16, v3
	v_add_u32_e32 v4, 0x100000, v3
	v_lshrrev_b32_e32 v5, 1, v2
	s_lshl_b32 s18, s15, 10
	v_add_u32_e32 v5, s18, v5
	v_and_b32_e32 v19, 63, v0
	v_lshrrev_b32_e32 v20, 6, v0
	s_waitcnt lgkmcnt(0)
	global_load_dwordx4 v[8:11], v3, s[4:5] nt
	global_load_dwordx4 v[12:15], v4, s[4:5] nt
	global_load_dword v6, v5, s[6:7]
	global_load_dword v16, v5, s[6:7] offset:512
	s_cmp_lt_u32 s14, 32
	s_cbranch_scc0 .Lprep_ld_done
	v_cmp_gt_u32_e32 vcc, 0x200, v0
	s_and_saveexec_b64 s[20:21], vcc
	s_cbranch_execz .Lprep_hb_skip
	v_lshrrev_b32_e32 v17, 5, v0
	v_and_b32_e32 v18, 31, v0
	v_lshlrev_b32_e32 v17, 12, v17
	v_lshl_or_b32 v17, v18, 2, v17
	v_add_u32_e32 v17, s17, v17
	global_load_dword v36, v17, s[10:11]
.Lprep_hb_skip:
	s_mov_b64 exec, s[20:21]
	s_cmp_lg_u32 s2, 0
	s_cbranch_scc1 .Lprep_ld_done
	v_lshlrev_b32_e32 v22, 2, v0
	global_load_dword v23, v22, s[6:7]
	global_load_dword v24, v22, s[8:9]
.Lprep_ld_done:
	s_getpc_b64 s[22:23]
	s_and_b32 s22, s22, 0xffffff00
	v_lshlrev_b32_e32 v25, 4, v0
	v_subrev_u32_e32 v30, 0x280, v0
	s_waitcnt vmcnt(0)
	s_movk_i32 s24, 0x240
	v_cmp_gt_u32_e32 vcc, s24, v0
	s_and_saveexec_b64 s[20:21], vcc
	s_cbranch_execz .Lprep_pf1
	global_load_dwordx4 v[26:29], v25, s[22:23]
.Lprep_pf1:
	s_mov_b64 exec, s[20:21]
	v_cmp_gt_u32_e32 vcc, 0x80, v30
	s_and_saveexec_b64 s[20:21], vcc
	s_cbranch_execz .Lprep_pf2
	s_and_b32 s24, s0, 0xffffffc0
	s_mov_b32 s25, s1
	v_lshlrev_b32_e32 v30, 4, v30
	v_add_u32_e32 v31, s24, v30
	v_xor_b32_e32 v31, s0, v31
	v_cmp_gt_u32_e32 vcc, 0x1000, v31
	s_and_b64 exec, exec, vcc
	s_cbranch_execz .Lprep_pf2
	global_load_dwordx4 v[32:35], v30, s[24:25]
.Lprep_pf2:
	s_mov_b64 exec, s[20:21]
	v_pk_mul_f32 v[12:13], v[12:13], v[16:17] op_sel_hi:[1,0]
	v_pk_mul_f32 v[14:15], v[14:15], v[16:17] op_sel_hi:[1,0]
	v_pk_fma_f32 v[8:9], v[8:9], v[6:7], v[12:13] op_sel_hi:[1,0,1]
	v_pk_fma_f32 v[10:11], v[10:11], v[6:7], v[14:15] op_sel_hi:[1,0,1]
	s_nop 1
	v_add_f32_dpp v8, v8, v8 row_ror:8 row_mask:0xf bank_mask:0xf bound_ctrl:1
	v_add_f32_dpp v9, v9, v9 row_ror:8 row_mask:0xf bank_mask:0xf bound_ctrl:1
	v_add_f32_dpp v10, v10, v10 row_ror:8 row_mask:0xf bank_mask:0xf bound_ctrl:1
	v_add_f32_dpp v11, v11, v11 row_ror:8 row_mask:0xf bank_mask:0xf bound_ctrl:1
	v_mov_b32_e32 v12, v8
	v_mov_b32_e32 v13, v9
	v_mov_b32_e32 v14, v10
	v_mov_b32_e32 v15, v11
	v_permlane16_swap_b32_e32 v8, v12
	v_permlane16_swap_b32_e32 v9, v13
	v_permlane16_swap_b32_e32 v10, v14
	v_permlane16_swap_b32_e32 v11, v15
	v_add_f32_e32 v8, v8, v12
	v_add_f32_e32 v9, v9, v13
	v_add_f32_e32 v10, v10, v14
	v_add_f32_e32 v11, v11, v15
	v_mov_b32_e32 v12, v8
	v_mov_b32_e32 v13, v9
	v_mov_b32_e32 v14, v10
	v_mov_b32_e32 v15, v11
	v_permlane32_swap_b32_e32 v8, v12
	v_permlane32_swap_b32_e32 v9, v13
	v_permlane32_swap_b32_e32 v10, v14
	v_permlane32_swap_b32_e32 v11, v15
	v_add_f32_e32 v8, v8, v12
	v_add_f32_e32 v9, v9, v13
	v_add_f32_e32 v10, v10, v14
	v_add_f32_e32 v11, v11, v15
	v_lshlrev_b32_e32 v21, 4, v19
	v_lshl_add_u32 v21, v20, 7, v21
	v_cmp_gt_u32_e32 vcc, 8, v19
	s_and_saveexec_b64 s[20:21], vcc
	ds_write_b128 v21, v[8:11]
	s_mov_b64 exec, s[20:21]
	s_cmp_lg_u32 s2, 0
	s_cbranch_scc1 .Lprep_bar
	v_mul_f32_e32 v23, v23, v24
	s_nop 1
	v_add_f32_dpp v23, v23, v23 quad_perm:[1,0,3,2] row_mask:0xf bank_mask:0xf bound_ctrl:1
	s_nop 1
	v_add_f32_dpp v23, v23, v23 quad_perm:[2,3,0,1] row_mask:0xf bank_mask:0xf bound_ctrl:1
	s_nop 1
	v_add_f32_dpp v23, v23, v23 row_ror:4 row_mask:0xf bank_mask:0xf bound_ctrl:1
	s_nop 1
	v_add_f32_dpp v23, v23, v23 row_ror:8 row_mask:0xf bank_mask:0xf bound_ctrl:1
	v_mov_b32_e32 v24, v23
	s_nop 1
	v_permlane16_swap_b32_e32 v23, v24
	v_add_f32_e32 v23, v23, v24
	v_mov_b32_e32 v24, v23
	s_nop 1
	v_permlane32_swap_b32_e32 v23, v24
	v_add_f32_e32 v23, v23, v24
	v_lshlrev_b32_e32 v22, 2, v20
	v_cmp_eq_u32_e32 vcc, 0, v19
	s_and_saveexec_b64 s[20:21], vcc
	ds_write_b32 v22, v23 offset:2048
	s_mov_b64 exec, s[20:21]
.Lprep_bar:
	s_waitcnt lgkmcnt(0)
	s_barrier
	s_cmp_lt_u32 s14, 32
	s_cbranch_scc1 .Lprep_hid
	v_cmp_gt_u32_e32 vcc, 32, v0
	s_and_saveexec_b64 s[20:21], vcc
	s_cbranch_execz .Lprep_done
	v_lshlrev_b32_e32 v1, 2, v0
	ds_read2_b32 v[2:3], v1 offset1:32
	ds_read2_b32 v[4:5], v1 offset0:64 offset1:96
	ds_read2_b32 v[6:7], v1 offset0:128 offset1:160
	ds_read2_b32 v[8:9], v1 offset0:192 offset1:224
	v_add_u32_e32 v10, 0x400, v1
	ds_read2_b32 v[12:13], v10 offset1:32
	ds_read2_b32 v[14:15], v10 offset0:64 offset1:96
	ds_read2_b32 v[16:17], v10 offset0:128 offset1:160
	ds_read2_b32 v[18:19], v10 offset0:192 offset1:224
	s_lshl_b32 s16, s15, 12
	s_add_i32 s16, s16, s17
	s_sub_i32 s16, s16, 0x1000
	v_add_u32_e32 v1, s16, v1
	s_waitcnt lgkmcnt(6)
	v_pk_add_f32 v[2:3], v[2:3], v[4:5]
	s_waitcnt lgkmcnt(4)
	v_pk_add_f32 v[6:7], v[6:7], v[8:9]
	s_waitcnt lgkmcnt(2)
	v_pk_add_f32 v[12:13], v[12:13], v[14:15]
	s_waitcnt lgkmcnt(0)
	v_pk_add_f32 v[16:17], v[16:17], v[18:19]
	v_pk_add_f32 v[2:3], v[2:3], v[6:7]
	v_pk_add_f32 v[12:13], v[12:13], v[16:17]
	s_nop 0
	v_pk_add_f32 v[2:3], v[2:3], v[12:13]
	s_nop 0
	v_add_f32_e32 v6, v2, v3
	global_store_dword v1, v6, s[12:13]
	s_endpgm
.Lprep_hid:
	v_cmp_gt_u32_e32 vcc, 0x200, v0
	s_and_saveexec_b64 s[20:21], vcc
	s_cbranch_execz .Lprep_done
	v_and_b32_e32 v37, 31, v0
	v_lshlrev_b32_e32 v1, 2, v37
	ds_read2_b32 v[2:3], v1 offset1:32
	ds_read2_b32 v[4:5], v1 offset0:64 offset1:96
	ds_read2_b32 v[6:7], v1 offset0:128 offset1:160
	ds_read2_b32 v[8:9], v1 offset0:192 offset1:224
	v_add_u32_e32 v10, 0x400, v1
	ds_read2_b32 v[12:13], v10 offset1:32
	ds_read2_b32 v[14:15], v10 offset0:64 offset1:96
	ds_read2_b32 v[16:17], v10 offset0:128 offset1:160
	ds_read2_b32 v[18:19], v10 offset0:192 offset1:224
	s_waitcnt lgkmcnt(6)
	v_pk_add_f32 v[2:3], v[2:3], v[4:5]
	s_waitcnt lgkmcnt(4)
	v_pk_add_f32 v[6:7], v[6:7], v[8:9]
	s_waitcnt lgkmcnt(2)
	v_pk_add_f32 v[12:13], v[12:13], v[14:15]
	s_waitcnt lgkmcnt(0)
	v_pk_add_f32 v[16:17], v[16:17], v[18:19]
	v_pk_add_f32 v[2:3], v[2:3], v[6:7]
	v_pk_add_f32 v[12:13], v[12:13], v[16:17]
	s_nop 0
	v_pk_add_f32 v[2:3], v[2:3], v[12:13]
	s_nop 0
	v_add_f32_e32 v6, v2, v3
	v_mul_f32_e32 v6, v36, v6
	s_nop 1
	v_add_f32_dpp v6, v6, v6 quad_perm:[1,0,3,2] row_mask:0xf bank_mask:0xf bound_ctrl:1
	s_nop 1
	v_add_f32_dpp v6, v6, v6 quad_perm:[2,3,0,1] row_mask:0xf bank_mask:0xf bound_ctrl:1
	s_nop 1
	v_add_f32_dpp v6, v6, v6 row_ror:4 row_mask:0xf bank_mask:0xf bound_ctrl:1
	s_nop 1
	v_add_f32_dpp v6, v6, v6 row_ror:8 row_mask:0xf bank_mask:0xf bound_ctrl:1
	v_mov_b32_e32 v7, v6
	s_nop 1
	v_permlane16_swap_b32_e32 v6, v7
	v_add_f32_e32 v6, v6, v7
	v_lshrrev_b32_e32 v2, 5, v0
	v_lshlrev_b32_e32 v2, 2, v2
	s_lshl_b32 s16, s15, 11
	s_lshl_b32 s18, s14, 6
	s_add_i32 s16, s16, s18
	s_addk_i32 s16, 0x4000
	v_add_u32_e32 v2, s16, v2
	v_cmp_eq_u32_e32 vcc, 0, v37
	s_and_saveexec_b64 s[22:23], vcc
	global_store_dword v2, v6, s[12:13]
	s_mov_b64 exec, s[22:23]
	s_cmp_lg_u32 s2, 0
	s_cbranch_scc1 .Lprep_done
	v_cmp_eq_u32_e32 vcc, 0, v0
	s_and_saveexec_b64 s[22:23], vcc
	s_cbranch_execz .Lprep_done
	v_mov_b32_e32 v1, 0x800
	ds_read_b128 v[2:5], v1
	ds_read_b128 v[6:9], v1 offset:16
	ds_read_b128 v[10:13], v1 offset:32
	ds_read_b128 v[14:17], v1 offset:48
	v_mov_b32_e32 v1, 0x6000
	s_waitcnt lgkmcnt(0)
	v_pk_add_f32 v[2:3], v[2:3], v[4:5]
	v_pk_add_f32 v[6:7], v[6:7], v[8:9]
	v_pk_add_f32 v[10:11], v[10:11], v[12:13]
	v_pk_add_f32 v[14:15], v[14:15], v[16:17]
	v_pk_add_f32 v[2:3], v[2:3], v[6:7]
	v_pk_add_f32 v[10:11], v[10:11], v[14:15]
	s_nop 0
	v_pk_add_f32 v[2:3], v[2:3], v[10:11]
	s_nop 0
	v_add_f32_e32 v2, v2, v3
	global_store_dword v1, v2, s[12:13]

	.amdhsa_kernel _Z11prep_kernelPKfS0_S0_S0_Pf
		.amdhsa_group_segment_fixed_size 2112
		.amdhsa_private_segment_fixed_size 0
		.amdhsa_kernarg_size 40
		.amdhsa_user_sgpr_count 2
		.amdhsa_user_sgpr_dispatch_ptr 0
		.amdhsa_user_sgpr_queue_ptr 0
		.amdhsa_user_sgpr_kernarg_segment_ptr 1
		.amdhsa_user_sgpr_dispatch_id 0
		.amdhsa_user_sgpr_kernarg_preload_length 0
		.amdhsa_user_sgpr_kernarg_preload_offset 0
		.amdhsa_user_sgpr_private_segment_size 0
		.amdhsa_uses_dynamic_stack 0
		.amdhsa_enable_private_segment 0
		.amdhsa_system_sgpr_workgroup_id_x 1
		.amdhsa_system_sgpr_workgroup_id_y 0
		.amdhsa_system_sgpr_workgroup_id_z 0
		.amdhsa_system_sgpr_workgroup_info 0
		.amdhsa_system_vgpr_workitem_id 0
		.amdhsa_next_free_vgpr 40
		.amdhsa_next_free_sgpr 26
		.amdhsa_accum_offset 40
		.amdhsa_reserve_vcc 1
		.amdhsa_float_round_mode_32 0
		.amdhsa_float_round_mode_16_64 0
		.amdhsa_float_denorm_mode_32 3
		.amdhsa_float_denorm_mode_16_64 3
		.amdhsa_dx10_clamp 1
		.amdhsa_ieee_mode 1
		.amdhsa_fp16_overflow 0
		.amdhsa_tg_split 0
		.amdhsa_exception_fp_ieee_invalid_op 0
		.amdhsa_exception_fp_denorm_src 0
		.amdhsa_exception_fp_ieee_div_zero 0
		.amdhsa_exception_fp_ieee_overflow 0
		.amdhsa_exception_fp_ieee_underflow 0
		.amdhsa_exception_fp_ieee_inexact 0
		.amdhsa_exception_int_div_zero 0
	.end_amdhsa_kernel

.Lfunc_end0:
	.size	_Z11prep_kernelPKfS0_S0_S0_Pf, .Lfunc_end0-_Z11prep_kernelPKfS0_S0_S0_Pf
	.set _Z11prep_kernelPKfS0_S0_S0_Pf.num_vgpr, 40
	.set _Z11prep_kernelPKfS0_S0_S0_Pf.num_agpr, 0
	.set _Z11prep_kernelPKfS0_S0_S0_Pf.numbered_sgpr, 26
	.set _Z11prep_kernelPKfS0_S0_S0_Pf.num_named_barrier, 0
	.set _Z11prep_kernelPKfS0_S0_S0_Pf.private_seg_size, 0
	.set _Z11prep_kernelPKfS0_S0_S0_Pf.uses_vcc, 1
	.set _Z11prep_kernelPKfS0_S0_S0_Pf.uses_flat_scratch, 0
	.set _Z11prep_kernelPKfS0_S0_S0_Pf.has_dyn_sized_stack, 0
	.set _Z11prep_kernelPKfS0_S0_S0_Pf.has_recursion, 0
	.set _Z11prep_kernelPKfS0_S0_S0_Pf.has_indirect_call, 0

amdhsa.kernels:
  - .agpr_count:     0
    .args:
      - .actual_access:  read_only
        .address_space:  global
        .offset:         0
        .size:           8
        .value_kind:     global_buffer
      - .actual_access:  read_only
        .address_space:  global
        .offset:         8
        .size:           8
        .value_kind:     global_buffer
      - .actual_access:  read_only
        .address_space:  global
        .offset:         16
        .size:           8
        .value_kind:     global_buffer
      - .actual_access:  read_only
        .address_space:  global
        .offset:         24
        .size:           8
        .value_kind:     global_buffer
      - .actual_access:  write_only
        .address_space:  global
        .offset:         32
        .size:           8
        .value_kind:     global_buffer
    .group_segment_fixed_size: 2112
    .kernarg_segment_align: 8
    .kernarg_segment_size: 40
    .language:       OpenCL C
    .language_version:
      - 2
      - 0
    .max_flat_workgroup_size: 1024
    .name:           _Z11prep_kernelPKfS0_S0_S0_Pf
    .private_segment_fixed_size: 0
    .sgpr_count:     32
    .sgpr_spill_count: 0
    .symbol:         _Z11prep_kernelPKfS0_S0_S0_Pf.kd
    .uniform_work_group_size: 1
    .uses_dynamic_stack: false
    .vgpr_count:     40
    .vgpr_spill_count: 0
    .wavefront_size: 64
  - .agpr_count:     0
    .args:
      - .actual_access:  read_only
        .address_space:  global
        .offset:         0
        .size:           8
        .value_kind:     global_buffer
      - .address_space:  global
        .offset:         8
        .size:           8
        .value_kind:     global_buffer
    .group_segment_fixed_size: 4096
    .kernarg_segment_align: 8
    .kernarg_segment_size: 16
    .language:       OpenCL C
    .language_version:
      - 2
      - 0
    .max_flat_workgroup_size: 1024
    .name:           _Z13stream_kernelPKfPf
    .private_segment_fixed_size: 0
    .sgpr_count:     17
    .sgpr_spill_count: 0
    .symbol:         _Z13stream_kernelPKfPf.kd
    .uniform_work_group_size: 1
    .uses_dynamic_stack: false
    .vgpr_count:     67
    .vgpr_spill_count: 0
    .wavefront_size: 64
  - .agpr_count:     0
    .args:
      - .actual_access:  read_only
        .address_space:  global
        .offset:         0
        .size:           8
        .value_kind:     global_buffer
      - .actual_access:  write_only
        .address_space:  global
        .offset:         8
        .size:           8
        .value_kind:     global_buffer
    .group_segment_fixed_size: 32
    .kernarg_segment_align: 8
    .kernarg_segment_size: 16
    .language:       OpenCL C
    .language_version:
      - 2
      - 0
    .max_flat_workgroup_size: 256
    .name:           _Z14softmax_kernelPKfPf
    .private_segment_fixed_size: 0
    .sgpr_count:     16
    .sgpr_spill_count: 0
    .symbol:         _Z14softmax_kernelPKfPf.kd
    .uniform_work_group_size: 1
    .uses_dynamic_stack: false
    .vgpr_count:     17
    .vgpr_spill_count: 0
    .wavefront_size: 64
